# speedup vs baseline: 1.0377x; 1.0100x over previous
_Z7k1_prepPKfPKiPiPfPDF16_S4_:
	s_load_dwordx2 s[4:5], s[0:1], 0x8
	v_mov_b32_e32 v39, 0
	v_lshlrev_b32_e32 v38, 4, v0
	s_movk_i32 s3, 0x2000
	v_and_b32_e32 v1, 63, v0
	s_waitcnt lgkmcnt(0)
	v_lshl_add_u64 v[18:19], s[4:5], 0, v[38:39]
	global_load_dwordx4 v[2:5], v38, s[4:5]
	v_add_co_u32_e32 v20, vcc, 0x1000, v18
	s_nop 1
	v_addc_co_u32_e32 v21, vcc, 0, v19, vcc
	global_load_dwordx4 v[22:25], v[20:21], off
	v_add_co_u32_e64 v6, s[4:5], s3, v18
	s_movk_i32 s3, 0x6000
	s_nop 0
	v_addc_co_u32_e64 v7, s[4:5], 0, v19, s[4:5]
	global_load_dwordx4 v[10:13], v[6:7], off
	v_add_co_u32_e32 v20, vcc, 0x3000, v18
	v_add_co_u32_e64 v30, s[4:5], s3, v18
	s_nop 0
	v_addc_co_u32_e32 v21, vcc, 0, v19, vcc
	v_addc_co_u32_e64 v31, s[4:5], 0, v19, s[4:5]
	s_movk_i32 s3, 0x7000
	global_load_dwordx4 v[26:29], v[20:21], off
	v_add_co_u32_e64 v14, s[4:5], s3, v18
	s_movk_i32 s3, 0x4000
	v_add_co_u32_e32 v18, vcc, s3, v18
	v_addc_co_u32_e64 v15, s[4:5], 0, v19, s[4:5]
	s_nop 0
	v_addc_co_u32_e32 v19, vcc, 0, v19, vcc
	global_load_dwordx4 v[14:17], v[14:15], off
	s_mov_b32 s3, 0x3f0000
	global_load_dwordx4 v[6:9], v[30:31], off offset:-4096
	v_cmp_eq_u32_e32 vcc, 0, v1
	global_load_dwordx4 v[18:21], v[18:19], off
	s_waitcnt vmcnt(6)
	v_mul_u32_u24_e32 v34, 6, v2
	global_load_dwordx4 v[30:33], v[30:31], off
	v_mul_u32_u24_e32 v36, 6, v3
	v_mul_u32_u24_e32 v40, 6, v4
	v_lshlrev_b64 v[34:35], v34, 1
	v_lshlrev_b64 v[36:37], v36, 1
	v_mul_u32_u24_e32 v42, 6, v5
	v_lshlrev_b64 v[40:41], v40, 1
	v_lshl_add_u64 v[34:35], v[34:35], 0, v[36:37]
	v_lshlrev_b64 v[42:43], v42, 1
	s_waitcnt vmcnt(6)
	v_mul_u32_u24_e32 v58, 6, v22
	v_lshl_add_u64 v[34:35], v[34:35], 0, v[40:41]
	v_mul_u32_u24_e32 v60, 6, v23
	v_lshlrev_b64 v[58:59], v58, 1
	v_lshl_add_u64 v[34:35], v[34:35], 0, v[42:43]
	v_mul_u32_u24_e32 v62, 6, v24
	v_lshlrev_b64 v[60:61], v60, 1
	v_lshl_add_u64 v[34:35], v[58:59], 0, v[34:35]
	v_mul_u32_u24_e32 v64, 6, v25
	v_lshlrev_b64 v[62:63], v62, 1
	v_lshl_add_u64 v[34:35], v[34:35], 0, v[60:61]
	s_waitcnt vmcnt(5)
	v_mul_u32_u24_e32 v36, 6, v10
	v_lshlrev_b64 v[64:65], v64, 1
	v_lshl_add_u64 v[34:35], v[34:35], 0, v[62:63]
	v_mul_u32_u24_e32 v44, 6, v11
	v_lshlrev_b64 v[36:37], v36, 1
	v_lshl_add_u64 v[34:35], v[34:35], 0, v[64:65]
	v_mul_u32_u24_e32 v45, 6, v12
	v_lshlrev_b64 v[40:41], v44, 1
	v_lshl_add_u64 v[34:35], v[36:37], 0, v[34:35]
	v_mul_u32_u24_e32 v46, 6, v13
	v_lshlrev_b64 v[44:45], v45, 1
	v_lshl_add_u64 v[34:35], v[34:35], 0, v[40:41]
	v_lshlrev_b64 v[46:47], v46, 1
	s_waitcnt vmcnt(4)
	v_mul_u32_u24_e32 v66, 6, v26
	v_lshl_add_u64 v[34:35], v[34:35], 0, v[44:45]
	v_mul_u32_u24_e32 v67, 6, v27
	v_lshlrev_b64 v[42:43], v66, 1
	v_lshl_add_u64 v[34:35], v[34:35], 0, v[46:47]
	v_mul_u32_u24_e32 v68, 6, v28
	v_lshlrev_b64 v[58:59], v67, 1
	v_lshl_add_u64 v[34:35], v[42:43], 0, v[34:35]
	v_mul_u32_u24_e32 v69, 6, v29
	v_lshlrev_b64 v[60:61], v68, 1
	v_lshl_add_u64 v[34:35], v[34:35], 0, v[58:59]
	v_lshlrev_b64 v[66:67], v69, 1
	v_lshl_add_u64 v[34:35], v[34:35], 0, v[60:61]
	s_waitcnt vmcnt(1)
	v_mul_u32_u24_e32 v44, 6, v18
	v_lshl_add_u64 v[34:35], v[34:35], 0, v[66:67]
	v_lshlrev_b64 v[44:45], v44, 1
	v_lshl_add_u64 v[34:35], v[44:45], 0, v[34:35]
	v_mul_u32_u24_e32 v44, 6, v19
	v_lshlrev_b64 v[44:45], v44, 1
	v_lshl_add_u64 v[34:35], v[34:35], 0, v[44:45]
	v_mul_u32_u24_e32 v44, 6, v20
	v_lshlrev_b64 v[44:45], v44, 1
	v_lshl_add_u64 v[34:35], v[34:35], 0, v[44:45]
	v_mul_u32_u24_e32 v44, 6, v21
	v_mul_u32_u24_e32 v48, 6, v6
	v_lshlrev_b64 v[44:45], v44, 1
	v_mul_u32_u24_e32 v56, 6, v7
	v_lshlrev_b64 v[48:49], v48, 1
	v_lshl_add_u64 v[34:35], v[34:35], 0, v[44:45]
	v_lshlrev_b64 v[56:57], v56, 1
	v_mul_u32_u24_e32 v36, 6, v8
	v_lshl_add_u64 v[34:35], v[48:49], 0, v[34:35]
	v_mul_u32_u24_e32 v50, 6, v9
	v_lshlrev_b64 v[36:37], v36, 1
	v_lshl_add_u64 v[34:35], v[34:35], 0, v[56:57]
	v_lshlrev_b64 v[50:51], v50, 1
	v_lshl_add_u64 v[34:35], v[34:35], 0, v[36:37]
	v_lshl_add_u64 v[34:35], v[34:35], 0, v[50:51]
	v_mul_u32_u24_e32 v52, 6, v14
	v_lshlrev_b64 v[52:53], v52, 1
	v_mul_u32_u24_e32 v40, 6, v15
	v_lshlrev_b64 v[40:41], v40, 1
	v_mul_u32_u24_e32 v42, 6, v16
	v_mul_u32_u24_e32 v54, 6, v17
	v_lshlrev_b64 v[42:43], v42, 1
	v_lshlrev_b64 v[54:55], v54, 1
	v_lshrrev_b32_e32 v44, 6, v0
	s_waitcnt vmcnt(0)
	v_mul_u32_u24_e32 v36, 6, v30
	v_lshlrev_b64 v[36:37], v36, 1
	v_lshl_add_u64 v[34:35], v[36:37], 0, v[34:35]
	v_mul_u32_u24_e32 v36, 6, v31
	v_lshlrev_b64 v[36:37], v36, 1
	v_lshl_add_u64 v[34:35], v[34:35], 0, v[36:37]
	v_mul_u32_u24_e32 v36, 6, v32
	v_lshlrev_b64 v[36:37], v36, 1
	v_lshl_add_u64 v[34:35], v[34:35], 0, v[36:37]
	v_mul_u32_u24_e32 v36, 6, v33
	v_lshlrev_b64 v[36:37], v36, 1
	v_lshl_add_u64 v[34:35], v[34:35], 0, v[36:37]
	v_lshl_add_u64 v[34:35], v[52:53], 0, v[34:35]
	v_lshl_add_u64 v[34:35], v[34:35], 0, v[40:41]
	v_lshl_add_u64 v[34:35], v[34:35], 0, v[42:43]
	v_lshl_add_u64 v[40:41], v[34:35], 0, v[54:55]
	v_lshlrev_b64 v[34:35], 20, v[40:41]
	v_and_b32_e32 v37, 63, v35
	v_lshlrev_b64 v[34:35], 30, v[40:41]
	v_and_b32_e32 v42, 0x3f0000, v35
	v_lshrrev_b64 v[34:35], 4, v[40:41]
	v_and_b32_e32 v45, 63, v35
	v_lshlrev_b64 v[34:35], 6, v[40:41]
	v_lshlrev_b32_e32 v36, 10, v40
	v_and_b32_e32 v34, 0x3f0000, v35
	v_and_b32_e32 v35, 63, v40
	v_and_or_b32 v35, v36, s3, v35
	v_or_b32_e32 v36, v37, v42
	v_bfe_u32 v37, v41, 16, 6
	v_add_u32_dpp v35, v35, v35 quad_perm:[1,0,3,2] row_mask:0xf bank_mask:0xf bound_ctrl:1
	v_lshrrev_b32_e32 v42, 6, v41
	v_alignbit_b32 v43, v41, v40, 14
	v_add_u32_dpp v35, v35, v35 quad_perm:[2,3,0,1] row_mask:0xf bank_mask:0xf bound_ctrl:1
	v_and_or_b32 v37, v42, s3, v37
	v_bfe_u32 v42, v40, 24, 6
	v_add_u32_dpp v35, v35, v35 row_half_mirror row_mask:0xf bank_mask:0xf bound_ctrl:1
	v_or_b32_e32 v34, v45, v34
	v_and_or_b32 v42, v43, s3, v42
	v_add_u32_dpp v35, v35, v35 row_mirror row_mask:0xf bank_mask:0xf bound_ctrl:1
	v_add_u32_dpp v34, v34, v34 quad_perm:[1,0,3,2] row_mask:0xf bank_mask:0xf bound_ctrl:1
	v_readlane_b32 s3, v35, 0
	v_readlane_b32 s6, v35, 16
	v_readlane_b32 s7, v35, 32
	v_readlane_b32 s8, v35, 48
	v_add_u32_dpp v35, v36, v36 quad_perm:[1,0,3,2] row_mask:0xf bank_mask:0xf bound_ctrl:1
	v_add_u32_dpp v34, v34, v34 quad_perm:[2,3,0,1] row_mask:0xf bank_mask:0xf bound_ctrl:1
	s_nop 0
	v_add_u32_dpp v35, v35, v35 quad_perm:[2,3,0,1] row_mask:0xf bank_mask:0xf bound_ctrl:1
	v_add_u32_dpp v34, v34, v34 row_half_mirror row_mask:0xf bank_mask:0xf bound_ctrl:1
	s_nop 0
	v_add_u32_dpp v35, v35, v35 row_half_mirror row_mask:0xf bank_mask:0xf bound_ctrl:1
	v_add_u32_dpp v34, v34, v34 row_mirror row_mask:0xf bank_mask:0xf bound_ctrl:1
	s_nop 0
	v_add_u32_dpp v35, v35, v35 row_mirror row_mask:0xf bank_mask:0xf bound_ctrl:1
	v_readlane_b32 s17, v34, 0
	v_readlane_b32 s10, v35, 0
	v_readlane_b32 s14, v35, 16
	v_readlane_b32 s15, v35, 32
	v_readlane_b32 s16, v35, 48
	v_add_u32_dpp v35, v42, v42 quad_perm:[1,0,3,2] row_mask:0xf bank_mask:0xf bound_ctrl:1
	v_readlane_b32 s18, v34, 16
	v_readlane_b32 s19, v34, 32
	v_readlane_b32 s20, v34, 48
	v_add_u32_dpp v34, v37, v37 quad_perm:[1,0,3,2] row_mask:0xf bank_mask:0xf bound_ctrl:1
	v_add_u32_dpp v35, v35, v35 quad_perm:[2,3,0,1] row_mask:0xf bank_mask:0xf bound_ctrl:1
	s_nop 0
	v_add_u32_dpp v34, v34, v34 quad_perm:[2,3,0,1] row_mask:0xf bank_mask:0xf bound_ctrl:1
	v_add_u32_dpp v35, v35, v35 row_half_mirror row_mask:0xf bank_mask:0xf bound_ctrl:1
	s_nop 0
	v_add_u32_dpp v34, v34, v34 row_half_mirror row_mask:0xf bank_mask:0xf bound_ctrl:1
	v_add_u32_dpp v35, v35, v35 row_mirror row_mask:0xf bank_mask:0xf bound_ctrl:1
	s_nop 0
	v_add_u32_dpp v34, v34, v34 row_mirror row_mask:0xf bank_mask:0xf bound_ctrl:1
	v_readlane_b32 s9, v35, 0
	v_readlane_b32 s11, v35, 16
	v_readlane_b32 s12, v35, 32
	v_readlane_b32 s13, v35, 48
	v_readlane_b32 s21, v34, 0
	v_readlane_b32 s22, v34, 16
	v_readlane_b32 s23, v34, 32
	v_readlane_b32 s24, v34, 48
	s_and_saveexec_b64 s[4:5], vcc
	s_cbranch_execz .LBB0_2
	s_add_i32 s3, s6, s3
	s_add_i32 s3, s3, s7
	s_add_i32 s10, s14, s10
	s_add_i32 s14, s3, s8
	s_add_i32 s3, s18, s17
	s_add_i32 s3, s3, s19
	s_add_i32 s7, s3, s20
	s_add_i32 s3, s11, s9
	s_add_i32 s3, s3, s12
	s_add_i32 s10, s10, s15
	s_add_i32 s6, s3, s13
	s_add_i32 s3, s22, s21
	v_mul_u32_u24_e32 v42, 24, v44
	s_add_i32 s15, s10, s16
	s_add_i32 s3, s3, s23
	v_or_b32_e32 v43, 0x5080, v42
	s_add_i32 s3, s3, s24
	v_mov_b64_e32 v[34:35], s[14:15]
	v_mov_b64_e32 v[36:37], s[6:7]
	v_mov_b32_e32 v46, s3
	v_mov_b32_e32 v47, v39
	ds_write2_b64 v43, v[34:35], v[36:37] offset1:1
	ds_write_b64 v42, v[46:47] offset:20624

.LBB0_33:
	s_and_b32 s2, s25, 0x1ff80
	s_add_i32 s2, s2, s39
	s_lshl_b32 s40, s20, 5
	s_cmp_ge_i32 s40, s2
	s_cbranch_scc1 .LBB0_63
	s_cmp_ge_u32 s40, s30
	s_cselect_b64 s[26:27], -1, 0
	s_cmp_lt_u32 s40, s31
	v_cndmask_b32_e64 v34, 0, 1, s[26:27]
	s_cselect_b64 s[2:3], -1, 0
	s_cmp_lt_u32 s40, s33
	v_cndmask_b32_e64 v34, 2, v34, s[2:3]
	s_cselect_b64 s[4:5], -1, 0
	s_cmp_lt_u32 s40, s34
	v_cndmask_b32_e64 v34, 3, v34, s[4:5]
	s_cselect_b64 s[6:7], -1, 0
	s_cmp_lt_u32 s40, s35
	v_cndmask_b32_e64 v34, 4, v34, s[6:7]
	s_cselect_b64 s[8:9], -1, 0
	s_cmp_lt_u32 s40, s36
	v_cndmask_b32_e64 v34, 5, v34, s[8:9]
	s_waitcnt lgkmcnt(0)
	s_cselect_b64 s[10:11], -1, 0
	s_cmp_lt_i32 s40, s37
	v_cndmask_b32_e64 v34, 6, v34, s[10:11]
	s_cselect_b64 s[12:13], -1, 0
	s_cmp_lt_i32 s40, s38
	v_cndmask_b32_e64 v34, 7, v34, s[12:13]
	s_cselect_b64 s[14:15], -1, 0
	s_cmp_lt_i32 s40, s39
	v_cndmask_b32_e64 v34, 8, v34, s[14:15]
	s_cselect_b64 s[16:17], -1, 0
	v_cndmask_b32_e64 v42, 9, v34, s[16:17]
	v_mul_u32_u24_e32 v34, 6, v42
	v_lshrrev_b64 v[34:35], v34, v[40:41]
	v_and_b32_e32 v46, 63, v34
	v_cmp_lt_u32_e64 s[18:19], 63, v0
	s_nop 0
	v_mov_b32_dpp v34, v46 row_shr:1 row_mask:0xf bank_mask:0xf bound_ctrl:1
	v_add_u32_e32 v36, v34, v46
	s_nop 1
	v_mov_b32_dpp v35, v36 row_shr:2 row_mask:0xf bank_mask:0xf bound_ctrl:1
	v_add_u32_e32 v37, v36, v35
	s_nop 1
	v_mov_b32_dpp v36, v37 row_shr:4 row_mask:0xf bank_mask:0xf bound_ctrl:1
	v_add_u32_e32 v39, v37, v36
	s_nop 1
	v_mov_b32_dpp v37, v39 row_shr:8 row_mask:0xf bank_mask:0xf bound_ctrl:1
	v_add_u32_e32 v47, v39, v37
	v_lshlrev_b32_e32 v39, 4, v42
	v_and_b32_e32 v40, 48, v39
	v_lshlrev_b32_e32 v39, 1, v42
	v_and_b32_e32 v39, -8, v39
	v_readlane_b32 s43, v47, 15
	v_readlane_b32 s42, v47, 31
	v_readlane_b32 s41, v47, 47
	v_add_u32_e32 v41, 0x5080, v39
	v_mov_b32_e32 v39, 0
	s_and_saveexec_b64 s[22:23], s[18:19]
	s_cbranch_execz .LBB0_36
	ds_read_b64 v[48:49], v41
	s_waitcnt lgkmcnt(0)
	v_lshrrev_b64 v[48:49], v40, v[48:49]
	v_and_b32_e32 v39, 0xffff, v48

.LBB0_46:
	s_or_b64 exec, exec, s[4:5]
	v_lshlrev_b32_e32 v2, 5, v44
	s_waitcnt lgkmcnt(0)
	s_barrier
	ds_read_b128 v[14:17], v2 offset:20480
	ds_read_b128 v[2:5], v2 offset:20496
	v_mov_b32_e32 v41, 0
	v_mov_b32_e32 v9, v41
	v_lshlrev_b32_e32 v40, 4, v1
	s_waitcnt lgkmcnt(1)
	v_mov_b32_e32 v8, v14
	v_lshlrev_b64 v[8:9], 6, v[8:9]
	v_cmp_gt_i32_e64 s[16:17], 0, v14
	v_mov_b32_e32 v10, v15
	v_mov_b32_e32 v11, v41
	v_lshl_add_u64 v[6:7], s[24:25], 0, v[40:41]
	v_cndmask_b32_e64 v9, v9, 0, s[16:17]
	v_cndmask_b32_e64 v8, v8, 0, s[16:17]
	v_lshlrev_b64 v[10:11], 6, v[10:11]
	v_cmp_gt_i32_e64 s[14:15], 0, v15
	v_lshl_add_u64 v[8:9], v[8:9], 4, v[6:7]
	v_cmp_gt_i32_e64 s[12:13], 0, v16
	v_cndmask_b32_e64 v11, v11, 0, s[14:15]
	v_cndmask_b32_e64 v10, v10, 0, s[14:15]
	v_lshl_add_u64 v[10:11], v[10:11], 4, v[6:7]
	global_load_dwordx4 v[48:51], v[8:9], off nt
	global_load_dwordx4 v[34:37], v[10:11], off nt
	v_mov_b32_e32 v8, v16
	v_mov_b32_e32 v9, v41
	v_lshlrev_b64 v[8:9], 6, v[8:9]
	v_mov_b32_e32 v10, v17
	v_mov_b32_e32 v11, v41
	v_cndmask_b32_e64 v9, v9, 0, s[12:13]
	v_cndmask_b32_e64 v8, v8, 0, s[12:13]
	v_lshlrev_b64 v[10:11], 6, v[10:11]
	v_cmp_gt_i32_e64 s[10:11], 0, v17
	v_lshl_add_u64 v[8:9], v[8:9], 4, v[6:7]
	s_waitcnt lgkmcnt(0)
	v_cmp_gt_i32_e64 s[8:9], 0, v2
	v_cndmask_b32_e64 v11, v11, 0, s[10:11]
	v_cndmask_b32_e64 v10, v10, 0, s[10:11]
	v_lshl_add_u64 v[10:11], v[10:11], 4, v[6:7]
	global_load_dwordx4 v[30:33], v[8:9], off nt
	global_load_dwordx4 v[26:29], v[10:11], off nt
	v_mov_b32_e32 v8, v2
	v_mov_b32_e32 v9, v41
	v_lshlrev_b64 v[8:9], 6, v[8:9]
	v_mov_b32_e32 v10, v3
	v_mov_b32_e32 v11, v41
	v_cndmask_b32_e64 v9, v9, 0, s[8:9]
	v_cndmask_b32_e64 v8, v8, 0, s[8:9]
	v_lshlrev_b64 v[10:11], 6, v[10:11]
	v_cmp_gt_i32_e64 s[6:7], 0, v3
	v_lshl_add_u64 v[8:9], v[8:9], 4, v[6:7]
	v_cmp_gt_i32_e64 s[4:5], 0, v4
	v_cndmask_b32_e64 v11, v11, 0, s[6:7]
	v_cndmask_b32_e64 v10, v10, 0, s[6:7]
	v_lshl_add_u64 v[10:11], v[10:11], 4, v[6:7]
	global_load_dwordx4 v[22:25], v[8:9], off nt
	global_load_dwordx4 v[18:21], v[10:11], off nt
	v_mov_b32_e32 v8, v4
	v_mov_b32_e32 v9, v41
	v_lshlrev_b64 v[8:9], 6, v[8:9]
	v_cndmask_b32_e64 v9, v9, 0, s[4:5]
	v_cndmask_b32_e64 v8, v8, 0, s[4:5]
	v_lshl_add_u64 v[42:43], v[8:9], 4, v[6:7]
	v_mov_b32_e32 v8, v5
	v_mov_b32_e32 v9, v41
	v_lshlrev_b64 v[8:9], 6, v[8:9]
	v_cmp_gt_i32_e64 s[2:3], 0, v5
	v_lshlrev_b32_e32 v1, 8, v0
	v_lshlrev_b32_e32 v0, 3, v0
	v_cndmask_b32_e64 v9, v9, 0, s[2:3]
	v_cndmask_b32_e64 v8, v8, 0, s[2:3]
	v_lshl_add_u64 v[46:47], v[8:9], 4, v[6:7]
	global_load_dwordx4 v[10:13], v[42:43], off nt
	global_load_dwordx4 v[6:9], v[46:47], off nt
	s_movk_i32 s19, 0x3c00
	v_and_b32_e32 v0, 8, v0
	v_and_or_b32 v46, v1, s19, v0
	s_mul_i32 s18, s20, 0x4080
	s_mul_hi_u32 s24, s20, 0x4080
	s_add_u32 s18, s22, s18
	v_lshlrev_b32_e32 v39, 3, v44
	v_and_b32_e32 v41, 32, v38
	s_addc_u32 s19, s23, s24
	s_add_u32 s22, s18, 0x4000
	s_addc_u32 s23, s19, 0
	v_add_u32_e32 v60, v39, v41
	v_lshl_add_u32 v60, v60, 4, v46
	v_mov_b32_e32 v66, 0x7f800000
	s_waitcnt vmcnt(7)
	v_cndmask_b32_e64 v48, v48, 0, s[16:17]
	v_cndmask_b32_e64 v49, v49, 0, s[16:17]
	v_cndmask_b32_e64 v50, v50, 0, s[16:17]
	v_cndmask_b32_e64 v51, v51, 0, s[16:17]
	v_pk_mul_f32 v[62:63], v[48:49], v[48:49]
	v_pk_mul_f32 v[64:65], v[50:51], v[50:51]
	v_add_f32_e32 v52, v62, v63
	v_add_f32_e32 v52, v52, v64
	v_add_f32_e32 v52, v52, v65
	v_cvt_pk_f16_f32 v62, v48, v49
	v_cvt_pk_f16_f32 v63, v50, v51
	ds_write_b64 v60, v[62:63]
	s_waitcnt vmcnt(6)
	v_cndmask_b32_e64 v34, v34, 0, s[14:15]
	v_cndmask_b32_e64 v35, v35, 0, s[14:15]
	v_cndmask_b32_e64 v36, v36, 0, s[14:15]
	v_cndmask_b32_e64 v37, v37, 0, s[14:15]
	v_pk_mul_f32 v[62:63], v[34:35], v[34:35]
	v_pk_mul_f32 v[64:65], v[36:37], v[36:37]
	v_add_f32_e32 v53, v62, v63
	v_add_f32_e32 v53, v53, v64
	v_add_f32_e32 v53, v53, v65
	v_cvt_pk_f16_f32 v62, v34, v35
	v_cvt_pk_f16_f32 v63, v36, v37
	ds_write_b64 v60, v[62:63] offset:16
	s_waitcnt vmcnt(5)
	v_cndmask_b32_e64 v30, v30, 0, s[12:13]
	v_cndmask_b32_e64 v31, v31, 0, s[12:13]
	v_cndmask_b32_e64 v32, v32, 0, s[12:13]
	v_cndmask_b32_e64 v33, v33, 0, s[12:13]
	v_pk_mul_f32 v[62:63], v[30:31], v[30:31]
	v_pk_mul_f32 v[64:65], v[32:33], v[32:33]
	v_add_f32_e32 v54, v62, v63
	v_add_f32_e32 v54, v54, v64
	v_add_f32_e32 v54, v54, v65
	v_cvt_pk_f16_f32 v62, v30, v31
	v_cvt_pk_f16_f32 v63, v32, v33
	ds_write_b64 v60, v[62:63] offset:32
	s_waitcnt vmcnt(4)
	v_cndmask_b32_e64 v26, v26, 0, s[10:11]
	v_cndmask_b32_e64 v27, v27, 0, s[10:11]
	v_cndmask_b32_e64 v28, v28, 0, s[10:11]
	v_cndmask_b32_e64 v29, v29, 0, s[10:11]
	v_pk_mul_f32 v[62:63], v[26:27], v[26:27]
	v_pk_mul_f32 v[64:65], v[28:29], v[28:29]
	v_add_f32_e32 v55, v62, v63
	v_add_f32_e32 v55, v55, v64
	v_add_f32_e32 v55, v55, v65
	v_cvt_pk_f16_f32 v62, v26, v27
	v_cvt_pk_f16_f32 v63, v28, v29
	ds_write_b64 v60, v[62:63] offset:48
	s_waitcnt vmcnt(3)
	v_cndmask_b32_e64 v22, v22, 0, s[8:9]
	v_cndmask_b32_e64 v23, v23, 0, s[8:9]
	v_cndmask_b32_e64 v24, v24, 0, s[8:9]
	v_cndmask_b32_e64 v25, v25, 0, s[8:9]
	v_pk_mul_f32 v[62:63], v[22:23], v[22:23]
	v_pk_mul_f32 v[64:65], v[24:25], v[24:25]
	v_add_f32_e32 v56, v62, v63
	v_add_f32_e32 v56, v56, v64
	v_add_f32_e32 v56, v56, v65
	v_cvt_pk_f16_f32 v62, v22, v23
	v_cvt_pk_f16_f32 v63, v24, v25
	ds_write_b64 v60, v[62:63] offset:64
	s_waitcnt vmcnt(2)
	v_cndmask_b32_e64 v18, v18, 0, s[6:7]
	v_cndmask_b32_e64 v19, v19, 0, s[6:7]
	v_cndmask_b32_e64 v20, v20, 0, s[6:7]
	v_cndmask_b32_e64 v21, v21, 0, s[6:7]
	v_pk_mul_f32 v[62:63], v[18:19], v[18:19]
	v_pk_mul_f32 v[64:65], v[20:21], v[20:21]
	v_add_f32_e32 v57, v62, v63
	v_add_f32_e32 v57, v57, v64
	v_add_f32_e32 v57, v57, v65
	v_cvt_pk_f16_f32 v62, v18, v19
	v_cvt_pk_f16_f32 v63, v20, v21
	ds_write_b64 v60, v[62:63] offset:80
	s_waitcnt vmcnt(1)
	v_cndmask_b32_e64 v10, v10, 0, s[4:5]
	v_cndmask_b32_e64 v11, v11, 0, s[4:5]
	v_cndmask_b32_e64 v12, v12, 0, s[4:5]
	v_cndmask_b32_e64 v13, v13, 0, s[4:5]
	v_pk_mul_f32 v[62:63], v[10:11], v[10:11]
	v_pk_mul_f32 v[64:65], v[12:13], v[12:13]
	v_add_f32_e32 v58, v62, v63
	v_add_f32_e32 v58, v58, v64
	v_add_f32_e32 v58, v58, v65
	v_cvt_pk_f16_f32 v62, v10, v11
	v_cvt_pk_f16_f32 v63, v12, v13
	ds_write_b64 v60, v[62:63] offset:96
	s_waitcnt vmcnt(0)
	v_cndmask_b32_e64 v6, v6, 0, s[2:3]
	v_cndmask_b32_e64 v7, v7, 0, s[2:3]
	v_cndmask_b32_e64 v8, v8, 0, s[2:3]
	v_cndmask_b32_e64 v9, v9, 0, s[2:3]
	v_pk_mul_f32 v[62:63], v[6:7], v[6:7]
	v_pk_mul_f32 v[64:65], v[8:9], v[8:9]
	v_add_f32_e32 v59, v62, v63
	v_add_f32_e32 v59, v59, v64
	v_add_f32_e32 v59, v59, v65
	v_cvt_pk_f16_f32 v62, v6, v7
	v_cvt_pk_f16_f32 v63, v8, v9
	ds_write_b64 v60, v[62:63] offset:112
	v_add_f32_dpp v52, v52, v52 quad_perm:[1,0,3,2] row_mask:0xf bank_mask:0xf bound_ctrl:1
	v_add_f32_dpp v53, v53, v53 quad_perm:[1,0,3,2] row_mask:0xf bank_mask:0xf bound_ctrl:1
	v_add_f32_dpp v54, v54, v54 quad_perm:[1,0,3,2] row_mask:0xf bank_mask:0xf bound_ctrl:1
	v_add_f32_dpp v55, v55, v55 quad_perm:[1,0,3,2] row_mask:0xf bank_mask:0xf bound_ctrl:1
	v_add_f32_dpp v56, v56, v56 quad_perm:[1,0,3,2] row_mask:0xf bank_mask:0xf bound_ctrl:1
	v_add_f32_dpp v57, v57, v57 quad_perm:[1,0,3,2] row_mask:0xf bank_mask:0xf bound_ctrl:1
	v_add_f32_dpp v58, v58, v58 quad_perm:[1,0,3,2] row_mask:0xf bank_mask:0xf bound_ctrl:1
	v_add_f32_dpp v59, v59, v59 quad_perm:[1,0,3,2] row_mask:0xf bank_mask:0xf bound_ctrl:1
	v_add_f32_dpp v52, v52, v52 quad_perm:[2,3,0,1] row_mask:0xf bank_mask:0xf bound_ctrl:1
	v_add_f32_dpp v53, v53, v53 quad_perm:[2,3,0,1] row_mask:0xf bank_mask:0xf bound_ctrl:1
	v_add_f32_dpp v54, v54, v54 quad_perm:[2,3,0,1] row_mask:0xf bank_mask:0xf bound_ctrl:1
	v_add_f32_dpp v55, v55, v55 quad_perm:[2,3,0,1] row_mask:0xf bank_mask:0xf bound_ctrl:1
	v_add_f32_dpp v56, v56, v56 quad_perm:[2,3,0,1] row_mask:0xf bank_mask:0xf bound_ctrl:1
	v_add_f32_dpp v57, v57, v57 quad_perm:[2,3,0,1] row_mask:0xf bank_mask:0xf bound_ctrl:1
	v_add_f32_dpp v58, v58, v58 quad_perm:[2,3,0,1] row_mask:0xf bank_mask:0xf bound_ctrl:1
	v_add_f32_dpp v59, v59, v59 quad_perm:[2,3,0,1] row_mask:0xf bank_mask:0xf bound_ctrl:1
	v_add_f32_dpp v52, v52, v52 row_half_mirror row_mask:0xf bank_mask:0xf bound_ctrl:1
	v_add_f32_dpp v53, v53, v53 row_half_mirror row_mask:0xf bank_mask:0xf bound_ctrl:1
	v_add_f32_dpp v54, v54, v54 row_half_mirror row_mask:0xf bank_mask:0xf bound_ctrl:1
	v_add_f32_dpp v55, v55, v55 row_half_mirror row_mask:0xf bank_mask:0xf bound_ctrl:1
	v_add_f32_dpp v56, v56, v56 row_half_mirror row_mask:0xf bank_mask:0xf bound_ctrl:1
	v_add_f32_dpp v57, v57, v57 row_half_mirror row_mask:0xf bank_mask:0xf bound_ctrl:1
	v_add_f32_dpp v58, v58, v58 row_half_mirror row_mask:0xf bank_mask:0xf bound_ctrl:1
	v_add_f32_dpp v59, v59, v59 row_half_mirror row_mask:0xf bank_mask:0xf bound_ctrl:1
	v_add_f32_dpp v52, v52, v52 row_mirror row_mask:0xf bank_mask:0xf bound_ctrl:1
	v_add_f32_dpp v53, v53, v53 row_mirror row_mask:0xf bank_mask:0xf bound_ctrl:1
	v_add_f32_dpp v54, v54, v54 row_mirror row_mask:0xf bank_mask:0xf bound_ctrl:1
	v_add_f32_dpp v55, v55, v55 row_mirror row_mask:0xf bank_mask:0xf bound_ctrl:1
	v_add_f32_dpp v56, v56, v56 row_mirror row_mask:0xf bank_mask:0xf bound_ctrl:1
	v_add_f32_dpp v57, v57, v57 row_mirror row_mask:0xf bank_mask:0xf bound_ctrl:1
	v_add_f32_dpp v58, v58, v58 row_mirror row_mask:0xf bank_mask:0xf bound_ctrl:1
	v_add_f32_dpp v59, v59, v59 row_mirror row_mask:0xf bank_mask:0xf bound_ctrl:1
	v_add_f32_dpp v52, v52, v52 row_bcast:15 row_mask:0xa bank_mask:0xf
	v_add_f32_dpp v53, v53, v53 row_bcast:15 row_mask:0xa bank_mask:0xf
	v_add_f32_dpp v54, v54, v54 row_bcast:15 row_mask:0xa bank_mask:0xf
	v_add_f32_dpp v55, v55, v55 row_bcast:15 row_mask:0xa bank_mask:0xf
	v_add_f32_dpp v56, v56, v56 row_bcast:15 row_mask:0xa bank_mask:0xf
	v_add_f32_dpp v57, v57, v57 row_bcast:15 row_mask:0xa bank_mask:0xf
	v_add_f32_dpp v58, v58, v58 row_bcast:15 row_mask:0xa bank_mask:0xf
	v_add_f32_dpp v59, v59, v59 row_bcast:15 row_mask:0xa bank_mask:0xf
	v_add_f32_dpp v52, v52, v52 row_bcast:31 row_mask:0xc bank_mask:0xf
	v_add_f32_dpp v53, v53, v53 row_bcast:31 row_mask:0xc bank_mask:0xf
	v_add_f32_dpp v54, v54, v54 row_bcast:31 row_mask:0xc bank_mask:0xf
	v_add_f32_dpp v55, v55, v55 row_bcast:31 row_mask:0xc bank_mask:0xf
	v_add_f32_dpp v56, v56, v56 row_bcast:31 row_mask:0xc bank_mask:0xf
	v_add_f32_dpp v57, v57, v57 row_bcast:31 row_mask:0xc bank_mask:0xf
	v_add_f32_dpp v58, v58, v58 row_bcast:31 row_mask:0xc bank_mask:0xf
	v_add_f32_dpp v59, v59, v59 row_bcast:31 row_mask:0xc bank_mask:0xf
	v_pk_add_f32 v[0:1], v[48:49], 0 op_sel_hi:[1,0]
	v_pk_add_f32 v[2:3], v[50:51], 0 op_sel_hi:[1,0]
	v_pk_add_f32 v[0:1], v[0:1], v[34:35]
	v_pk_add_f32 v[2:3], v[2:3], v[36:37]
	v_pk_add_f32 v[0:1], v[0:1], v[30:31]
	v_pk_add_f32 v[2:3], v[2:3], v[32:33]
	v_pk_add_f32 v[0:1], v[0:1], v[26:27]
	v_pk_add_f32 v[2:3], v[2:3], v[28:29]
	v_pk_add_f32 v[0:1], v[0:1], v[22:23]
	v_pk_add_f32 v[2:3], v[2:3], v[24:25]
	v_pk_add_f32 v[0:1], v[0:1], v[18:19]
	v_pk_add_f32 v[2:3], v[2:3], v[20:21]
	v_pk_add_f32 v[0:1], v[0:1], v[10:11]
	v_pk_add_f32 v[2:3], v[2:3], v[12:13]
	v_pk_add_f32 v[0:1], v[0:1], v[6:7]
	v_pk_add_f32 v[2:3], v[2:3], v[8:9]
	s_mov_b64 s[24:25], exec
	s_mov_b32 exec_lo, 0
	s_brev_b32 exec_hi, 1
	v_cndmask_b32_e64 v52, v52, v66, s[16:17]
	v_cndmask_b32_e64 v53, v53, v66, s[14:15]
	v_cndmask_b32_e64 v54, v54, v66, s[12:13]
	v_cndmask_b32_e64 v55, v55, v66, s[10:11]
	v_cndmask_b32_e64 v56, v56, v66, s[8:9]
	v_cndmask_b32_e64 v57, v57, v66, s[6:7]
	v_cndmask_b32_e64 v58, v58, v66, s[4:5]
	v_cndmask_b32_e64 v59, v59, v66, s[2:3]
	v_lshlrev_b32_e32 v61, 2, v39
	global_store_dwordx4 v61, v[52:55], s[22:23]
	global_store_dwordx4 v61, v[56:59], s[22:23] offset:16
	s_mov_b64 exec, s[24:25]
	s_load_dwordx2 s[6:7], s[0:1], 0x18
	v_lshl_or_b32 v4, v44, 10, v40
	ds_write_b128 v4, v[0:3] offset:16384
	s_waitcnt lgkmcnt(0)
	s_barrier
	ds_read_b128 v[0:3], v38
	ds_read_b128 v[4:7], v38 offset:4096
	v_mov_b32_e32 v39, 0
	v_lshl_add_u64 v[8:9], s[18:19], 0, v[38:39]
	s_movk_i32 s0, 0x2000
	s_waitcnt lgkmcnt(1)
	global_store_dwordx4 v38, v[0:3], s[18:19]
	ds_read_b128 v[0:3], v38 offset:8192
	v_add_co_u32_e32 v10, vcc, s0, v8
	s_movk_i32 s0, 0x3000
	s_nop 0
	v_addc_co_u32_e32 v11, vcc, 0, v9, vcc
	s_waitcnt lgkmcnt(1)
	global_store_dwordx4 v[10:11], v[4:7], off offset:-4096
	ds_read_b128 v[4:7], v38 offset:12288
	s_waitcnt lgkmcnt(1)
	global_store_dwordx4 v[10:11], v[0:3], off
	ds_read2st64_b32 v[0:1], v45 offset0:64 offset1:68
	ds_read2st64_b32 v[2:3], v45 offset0:72 offset1:76
	v_add_co_u32_e32 v8, vcc, s0, v8
	s_lshl_b64 s[0:1], s[20:21], 10
	s_waitcnt lgkmcnt(1)
	v_add_f32_e32 v0, v0, v1
	s_waitcnt lgkmcnt(0)
	v_add_f32_e32 v0, v0, v2
	s_add_u32 s0, s6, s0
	v_addc_co_u32_e32 v9, vcc, 0, v9, vcc
	v_add_f32_e32 v0, v0, v3
	s_addc_u32 s1, s7, s1
	global_store_dwordx4 v[8:9], v[4:7], off
	global_store_dword v45, v0, s[0:1]
